# warm
# speedup vs baseline: 1.0413x; 1.0413x over previous
_Z11prep_kernelPKfS0_PKiS2_S0_S0_S0_S0_S0_S0_Pc:
	s_getpc_b64 s[36:37]
	s_add_u32 s36, s36, _Z11attn_kernelILi4EEvPKfS1_S1_S1_S1_S1_PKcPf@rel32@lo+4
	s_addc_u32 s37, s37, _Z11attn_kernelILi4EEvPKfS1_S1_S1_S1_S1_PKcPf@rel32@hi+12
	v_and_b32_e32 v192, 63, v0
	v_lshlrev_b32_e32 v192, 7, v192
	v_min_u32_e32 v192, 0x1180, v192
	global_load_dword v192, v192, s[36:37]
	s_lshr_b32 s4, s2, 2
	v_lshrrev_b32_e32 v2, 6, v0
	s_and_b32 s4, s4, 0x1ffffffe
	s_load_dwordx4 s[28:31], s[0:1], 0x40
	s_load_dwordx8 s[12:19], s[0:1], 0x0
	s_load_dwordx8 s[20:27], s[0:1], 0x20
	s_load_dwordx2 s[32:33], s[0:1], 0x50
	v_and_b32_e32 v1, 15, v0
	s_and_b32 s3, s2, 7
	v_or_b32_e32 v2, s4, v2
	v_lshl_or_b32 v88, v2, 3, s3
	v_cmp_gt_u32_e64 s[10:11], 14, v1
	v_mul_lo_u32 v7, v88, 14
	v_and_b32_e32 v105, 63, v0
	v_cndmask_b32_e64 v6, 13, v1, s[10:11]
	v_add_u32_e32 v2, v7, v6
	v_mul_u32_u24_e32 v4, 12, v2
	v_lshlrev_b32_e32 v5, 2, v6
	v_cmp_gt_u32_e64 s[8:9], 48, v105
	v_cmp_gt_u32_e64 s[6:7], 14, v105
	v_lshlrev_b32_e32 v118, 1, v0
	v_lshrrev_b32_e32 v104, 4, v0
	v_cndmask_b32_e64 v8, 0, v105, s[8:9]
	v_cndmask_b32_e64 v9, 0, v105, s[6:7]
	v_mad_u32_u24 v8, v88, 48, v8
	v_add_lshl_u32 v9, v7, v9, 2
	v_lshlrev_b32_e32 v8, 2, v8
	s_lshl_b32 s2, s2, 3
	s_and_b32 s2, s2, 0x78
	v_and_b32_e32 v106, 30, v118
	v_or_b32_e32 v107, s2, v104
	v_cmp_gt_u32_e64 s[2:3], 23, v106
	v_or_b32_e32 v10, 1, v106
	v_cmp_gt_u32_e64 s[4:5], 23, v10
	v_lshlrev_b32_e32 v11, 7, v106
	v_lshlrev_b32_e32 v10, 7, v10
	v_cndmask_b32_e64 v11, 0, v11, s[2:3]
	v_cndmask_b32_e64 v10, 0, v10, s[4:5]
	v_or_b32_e32 v11, v11, v107
	v_or_b32_e32 v10, v10, v107
	v_lshlrev_b32_e32 v11, 2, v11
	v_lshlrev_b32_e32 v10, 2, v10
	v_lshlrev_b32_e32 v12, 2, v107
	v_lshlrev_b32_e32 v119, 5, v0
	v_lshlrev_b32_e32 v13, 2, v0
	v_and_b32_e32 v109, 12, v13
	v_and_b32_e32 v91, 0xf80, v119
	v_lshl_or_b32 v91, v109, 2, v91
	v_or_b32_e32 v92, 0x1000, v91
	v_lshlrev_b32_e32 v90, 9, v2
	v_and_b32_e32 v16, 48, v0
	v_or_b32_e32 v90, v90, v16
	v_or_b32_e32 v112, 0x80, v0
	v_or_b32_e32 v111, 0x180, v0
	v_or_b32_e32 v108, 0x280, v0
	v_mov_b32_e32 v87, 0
	v_bfe_u32 v110, v0, 4, 2
	s_movk_i32 s34, 0x60
	v_lshrrev_b32_e32 v136, 1, v0
	v_lshrrev_b32_e32 v18, 3, v0
	v_and_b32_e32 v18, 4, v18
	v_and_b32_e32 v19, 24, v0
	v_and_b32_e32 v20, 2, v136
	v_or3_b32 v18, v18, v19, v20
	v_and_or_b32 v136, v136, s34, v18
	v_mul_u32_u24_e32 v18, 0x110, v109
	v_lshl_add_u32 v136, v136, 1, v18
	v_add_u32_e32 v137, 0x1100, v136
	v_add_u32_e32 v138, 0x2200, v136
	v_lshlrev_b32_e32 v18, 9, v88
	v_and_b32_e32 v19, 0x100, v119
	v_lshlrev_b32_e32 v20, 4, v0
	v_and_b32_e32 v20, 48, v20
	v_or3_b32 v139, v18, v19, v20
	v_and_b32_e32 v19, 8, v118
	v_and_b32_e32 v20, 64, v118
	v_or3_b32 v139, v139, v19, v20
	v_lshlrev_b32_e32 v19, 2, v110
	v_and_b32_e32 v20, 4, v19
	v_or_b32_e32 v139, v139, v20
	v_lshl_or_b32 v140, v1, 5, v18
	v_or_b32_e32 v140, v140, v19
	v_add_u32_e32 v140, 0x80000, v140
	v_lshl_or_b32 v141, v88, 4, v1
	v_lshlrev_b32_e32 v141, 3, v141
	v_add_u32_e32 v141, 0x140000, v141
	v_lshlrev_b32_e32 v20, 8, v88
	v_mul_u32_u24_e32 v21, 43, v105
	v_lshrrev_b32_e32 v21, 9, v21
	v_mul_u32_u24_e32 v21, 12, v21
	v_sub_u32_e32 v22, v105, v21
	v_and_b32_e32 v142, 3, v22
	v_lshrrev_b32_e32 v22, 2, v22
	v_mad_u32_u24 v142, v142, 3, v22
	v_add_u32_e32 v142, v142, v21
	v_lshl_add_u32 v142, v142, 2, v20
	v_add_u32_e32 v142, 0x164000, v142
	v_lshl_add_u32 v143, v105, 2, v20
	v_add_u32_e32 v143, 0x164000, v143
	v_lshlrev_b32_e32 v123, 6, v107
	v_lshl_add_u32 v123, v106, 1, v123
	v_add_u32_e32 v123, 0x160000, v123
	v_lshl_add_u32 v122, v1, 4, v20
	v_or_b32_e32 v122, v122, v19
	v_add_u32_e32 v122, 0x100000, v122
	s_waitcnt lgkmcnt(0)
	global_load_dwordx3 v[82:84], v4, s[12:13]
	global_load_dword v85, v5, s[26:27]
	global_load_dword v114, v8, s[18:19]
	global_load_dword v115, v9, s[16:17]
	global_load_dword v116, v11, s[28:29]
	global_load_dword v113, v10, s[28:29]
	global_load_dword v117, v12, s[30:31]
	global_load_dwordx4 v[66:69], v91, s[20:21]
	global_load_dwordx4 v[70:73], v91, s[20:21] offset:64
	global_load_dwordx4 v[74:77], v92, s[20:21]
	global_load_dwordx4 v[78:81], v92, s[20:21] offset:64
	global_load_dwordx4 v[58:61], v91, s[22:23]
	global_load_dwordx4 v[62:65], v91, s[22:23] offset:64
	global_load_dwordx4 v[50:53], v92, s[22:23]
	global_load_dwordx4 v[54:57], v92, s[22:23] offset:64
	global_load_dwordx4 v[42:45], v91, s[24:25]
	global_load_dwordx4 v[46:49], v91, s[24:25] offset:64
	global_load_dwordx4 v[34:37], v92, s[24:25]
	global_load_dwordx4 v[38:41], v92, s[24:25] offset:64
	global_load_dwordx4 v[26:29], v90, s[14:15] nt
	global_load_dwordx4 v[30:33], v90, s[14:15] offset:64 nt
	global_load_dwordx4 v[18:21], v90, s[14:15] offset:128 nt
	global_load_dwordx4 v[22:25], v90, s[14:15] offset:192 nt
	global_load_dwordx4 v[10:13], v90, s[14:15] offset:256 nt
	global_load_dwordx4 v[14:17], v90, s[14:15] offset:320 nt
	global_load_dwordx4 v[2:5], v90, s[14:15] offset:384 nt
	global_load_dwordx4 v[6:9], v90, s[14:15] offset:448 nt
	s_waitcnt vmcnt(26)
	v_mov_b32_e32 v90, v83
	v_mov_b32_e32 v91, v84
	v_lshlrev_b32_e32 v86, 2, v110
	s_waitcnt vmcnt(25)
	v_mul_f32_e32 v84, 0x3fb8aa3b, v85
	s_mov_b32 s14, 0x41700000
	v_exp_f32_e32 v84, v84
	v_cndmask_b32_e64 v94, 0, 1.0, s[10:11]
	v_add_f32_e32 v84, 1.0, v84
	v_cmp_lt_f32_e32 vcc, s14, v85
	v_log_f32_e32 v84, v84
	v_cmp_lt_u32_e64 s[12:13], 15, v105
	v_mul_f32_e32 v84, 0x3f317218, v84
	v_cndmask_b32_e32 v84, v84, v85, vcc
	v_mul_f32_e32 v84, 0xbe715bef, v84
	v_mul_f32_e32 v84, 0x3f3504f3, v84
	v_mul_f32_e32 v84, 0x41800000, v84
	v_cndmask_b32_e64 v99, 0, v84, s[10:11]
	v_mul_f32_e32 v101, -2.0, v99
	v_mul_f32_e32 v100, v82, v82
	v_cmp_gt_u32_e32 vcc, 16, v105
	v_fmac_f32_e32 v100, v90, v90
	v_cmp_eq_u32_e64 s[12:13], 0, v110
	v_fmac_f32_e32 v100, v91, v91
	v_cmp_eq_u32_e64 s[14:15], 1, v110
	v_mul_f32_e32 v83, v101, v82
	v_cmp_eq_u32_e64 s[16:17], 2, v110
	v_mul_f32_e32 v84, v101, v90
	v_mul_f32_e32 v85, v101, v91
	v_mul_f32_e32 v89, v99, v100
	v_mul_f32_e32 v92, v82, v94
	v_mul_f32_e32 v93, v90, v94
	v_mul_f32_e32 v95, v91, v94
	v_mul_f32_e32 v96, v100, v94
	v_cvt_pk_fp8_f32 v88, v83, v83
	v_cvt_pk_fp8_f32 v104, v84, v84
	v_cvt_f32_fp8_e32 v97, v88
	v_cvt_f32_fp8_e32 v98, v104
	v_sub_f32_e32 v97, v83, v97
	v_sub_f32_e32 v98, v84, v98
	v_cvt_pk_fp8_f32 v88, v85, v85
	v_cvt_pk_fp8_f32 v104, v99, v99
	v_cvt_f32_fp8_e32 v101, v88
	v_cvt_f32_fp8_e32 v102, v104
	v_sub_f32_e32 v101, v85, v101
	v_sub_f32_e32 v102, v99, v102
	v_cvt_pk_fp8_f32 v88, v89, v89
	v_cvt_pk_fp8_f32 v104, v92, v92
	v_cvt_f32_fp8_e32 v103, v88
	v_cvt_f32_fp8_e32 v120, v104
	v_sub_f32_e32 v103, v89, v103
	v_sub_f32_e32 v120, v92, v120
	v_cvt_pk_fp8_f32 v88, v93, v93
	v_cvt_pk_fp8_f32 v104, v95, v95
	v_cvt_f32_fp8_e32 v121, v88
	v_cvt_f32_fp8_e32 v86, v104
	v_sub_f32_e32 v121, v93, v121
	v_sub_f32_e32 v86, v95, v86
	v_cvt_pk_fp8_f32 v88, v96, v96
	s_nop 0
	v_cvt_f32_fp8_e32 v87, v88
	s_nop 0
	v_sub_f32_e32 v87, v96, v87
	v_cndmask_b32_e64 v124, v89, v85, s[16:17]
	v_cndmask_b32_e64 v124, v124, v98, s[14:15]
	v_cndmask_b32_e64 v124, v124, v83, s[12:13]
	v_cndmask_b32_e64 v125, v103, v99, s[16:17]
	v_cndmask_b32_e64 v125, v125, v84, s[14:15]
	v_cndmask_b32_e64 v125, v125, v97, s[12:13]
	v_cndmask_b32_e64 v126, 0, v102, s[16:17]
	v_cndmask_b32_e64 v126, v126, v85, s[14:15]
	v_cndmask_b32_e64 v126, v126, v83, s[12:13]
	v_cndmask_b32_e64 v127, 0, v99, s[16:17]
	v_cndmask_b32_e64 v127, v127, v101, s[14:15]
	v_cndmask_b32_e64 v127, v127, v84, s[12:13]
	v_cndmask_b32_e64 v128, v94, v86, s[16:17]
	v_cndmask_b32_e64 v128, v128, v93, s[14:15]
	v_cndmask_b32_e64 v128, v128, v92, s[12:13]
	v_cndmask_b32_e64 v129, v94, v96, s[16:17]
	v_cndmask_b32_e64 v129, v129, v121, s[14:15]
	v_cndmask_b32_e64 v129, v129, v92, s[12:13]
	v_cndmask_b32_e64 v130, 0, v96, s[16:17]
	v_cndmask_b32_e64 v130, v130, v95, s[14:15]
	v_cndmask_b32_e64 v130, v130, v120, s[12:13]
	v_cndmask_b32_e64 v131, 0, v87, s[16:17]
	v_cndmask_b32_e64 v131, v131, v95, s[14:15]
	v_cndmask_b32_e64 v131, v131, v93, s[12:13]
	v_cvt_pk_fp8_f32 v119, v124, v125
	v_cvt_pk_fp8_f32 v103, v128, v129
	v_cvt_pk_fp8_f32 v119, v126, v127 op_sel:[0,0,1]
	v_cvt_pk_fp8_f32 v103, v130, v131 op_sel:[0,0,1]
	s_nop 0
	global_store_dword v139, v119, s[32:33] offset:128
	global_store_dword v140, v103, s[32:33] offset:16
	s_and_saveexec_b64 s[0:1], vcc
	s_cbranch_execz .LBB0_14
	v_cvt_f16_f32_e32 v83, v82
	v_cvt_pk_f16_f32 v90, v90, v91
	s_nop 0
	v_alignbit_b32 v91, 0, v90, 16
	v_pack_b32_f16 v90, v83, v90
	global_store_dwordx2 v141, v[90:91], s[32:33]

	.amdhsa_kernel _Z11prep_kernelPKfS0_PKiS2_S0_S0_S0_S0_S0_S0_Pc
		.amdhsa_group_segment_fixed_size 13056
		.amdhsa_private_segment_fixed_size 0
		.amdhsa_kernarg_size 88
		.amdhsa_user_sgpr_count 2
		.amdhsa_user_sgpr_dispatch_ptr 0
		.amdhsa_user_sgpr_queue_ptr 0
		.amdhsa_user_sgpr_kernarg_segment_ptr 1
		.amdhsa_user_sgpr_dispatch_id 0
		.amdhsa_user_sgpr_kernarg_preload_length 0
		.amdhsa_user_sgpr_kernarg_preload_offset 0
		.amdhsa_user_sgpr_private_segment_size 0
		.amdhsa_uses_dynamic_stack 0
		.amdhsa_enable_private_segment 0
		.amdhsa_system_sgpr_workgroup_id_x 1
		.amdhsa_system_sgpr_workgroup_id_y 0
		.amdhsa_system_sgpr_workgroup_id_z 0
		.amdhsa_system_sgpr_workgroup_info 0
		.amdhsa_system_vgpr_workitem_id 0
		.amdhsa_next_free_vgpr 200
		.amdhsa_next_free_sgpr 91
		.amdhsa_accum_offset 200
		.amdhsa_reserve_vcc 1
		.amdhsa_float_round_mode_32 0
		.amdhsa_float_round_mode_16_64 0
		.amdhsa_float_denorm_mode_32 3
		.amdhsa_float_denorm_mode_16_64 3
		.amdhsa_dx10_clamp 1
		.amdhsa_ieee_mode 1
		.amdhsa_fp16_overflow 0
		.amdhsa_tg_split 0
		.amdhsa_exception_fp_ieee_invalid_op 0
		.amdhsa_exception_fp_denorm_src 0
		.amdhsa_exception_fp_ieee_div_zero 0
		.amdhsa_exception_fp_ieee_overflow 0
		.amdhsa_exception_fp_ieee_underflow 0
		.amdhsa_exception_fp_ieee_inexact 0
		.amdhsa_exception_int_div_zero 0
	.end_amdhsa_kernel

amdhsa.kernels:
  - .agpr_count:     0
    .args:
      - .actual_access:  read_only
        .address_space:  global
        .offset:         0
        .size:           8
        .value_kind:     global_buffer
      - .actual_access:  read_only
        .address_space:  global
        .offset:         8
        .size:           8
        .value_kind:     global_buffer
      - .actual_access:  read_only
        .address_space:  global
        .offset:         16
        .size:           8
        .value_kind:     global_buffer
      - .actual_access:  read_only
        .address_space:  global
        .offset:         24
        .size:           8
        .value_kind:     global_buffer
      - .actual_access:  read_only
        .address_space:  global
        .offset:         32
        .size:           8
        .value_kind:     global_buffer
      - .actual_access:  read_only
        .address_space:  global
        .offset:         40
        .size:           8
        .value_kind:     global_buffer
      - .actual_access:  read_only
        .address_space:  global
        .offset:         48
        .size:           8
        .value_kind:     global_buffer
      - .actual_access:  read_only
        .address_space:  global
        .offset:         56
        .size:           8
        .value_kind:     global_buffer
      - .actual_access:  read_only
        .address_space:  global
        .offset:         64
        .size:           8
        .value_kind:     global_buffer
      - .actual_access:  read_only
        .address_space:  global
        .offset:         72
        .size:           8
        .value_kind:     global_buffer
      - .actual_access:  write_only
        .address_space:  global
        .offset:         80
        .size:           8
        .value_kind:     global_buffer
    .group_segment_fixed_size: 13056
    .kernarg_segment_align: 8
    .kernarg_segment_size: 88
    .language:       OpenCL C
    .language_version:
      - 2
      - 0
    .max_flat_workgroup_size: 128
    .name:           _Z11prep_kernelPKfS0_PKiS2_S0_S0_S0_S0_S0_S0_Pc
    .private_segment_fixed_size: 0
    .sgpr_count:     41
    .sgpr_spill_count: 0
    .symbol:         _Z11prep_kernelPKfS0_PKiS2_S0_S0_S0_S0_S0_S0_Pc.kd
    .uniform_work_group_size: 1
    .uses_dynamic_stack: false
    .vgpr_count:     200
    .vgpr_spill_count: 0
    .wavefront_size: 64
  - .agpr_count:     0
    .args:
      - .actual_access:  read_only
        .address_space:  global
        .offset:         0
        .size:           8
        .value_kind:     global_buffer
      - .actual_access:  read_only
        .address_space:  global
        .offset:         8
        .size:           8
        .value_kind:     global_buffer
      - .actual_access:  read_only
        .address_space:  global
        .offset:         16
        .size:           8
        .value_kind:     global_buffer
      - .actual_access:  read_only
        .address_space:  global
        .offset:         24
        .size:           8
        .value_kind:     global_buffer
      - .actual_access:  read_only
        .address_space:  global
        .offset:         32
        .size:           8
        .value_kind:     global_buffer
      - .actual_access:  read_only
        .address_space:  global
        .offset:         40
        .size:           8
        .value_kind:     global_buffer
      - .actual_access:  read_only
        .address_space:  global
        .offset:         48
        .size:           8
        .value_kind:     global_buffer
      - .actual_access:  write_only
        .address_space:  global
        .offset:         56
        .size:           8
        .value_kind:     global_buffer
    .group_segment_fixed_size: 16640
    .kernarg_segment_align: 8
    .kernarg_segment_size: 64
    .language:       OpenCL C
    .language_version:
      - 2
      - 0
    .max_flat_workgroup_size: 256
    .name:           _Z11attn_kernelILi4EEvPKfS1_S1_S1_S1_S1_PKcPf
    .private_segment_fixed_size: 0
    .sgpr_count:     38
    .sgpr_spill_count: 0
    .symbol:         _Z11attn_kernelILi4EEvPKfS1_S1_S1_S1_S1_PKcPf.kd
    .uniform_work_group_size: 1
    .uses_dynamic_stack: false
    .vgpr_count:     256
    .vgpr_spill_count: 0
    .wavefront_size: 64
